# P0 xn row loop: next row's loads issued before the current row is processed (copy through spare VGPRs), stacked on previous
# speedup vs baseline: 1.0038x; 1.0038x over previous
.LBB0_11:
	s_cmpk_lt_i32 s10, 0x4000
	s_cbranch_scc0 .LBB0_14
	v_and_b32_e32 v38, 63, v0
	v_lshlrev_b32_e32 v34, 5, v38
	v_mov_b32_e32 v35, 0
	v_lshl_add_u64 v[18:19], s[70:71], 0, v[34:35]
	s_mov_b64 s[4:5], 0x1800
	v_lshl_add_u64 v[30:31], v[18:19], 0, s[4:5]
	s_movk_i32 s4, 0x1000
	s_mov_b64 s[2:3], 0x1000
	v_add_co_u32_e32 v22, vcc, s4, v18
	v_lshl_add_u64 v[26:27], v[18:19], 0, s[2:3]
	s_nop 0
	v_addc_co_u32_e32 v23, vcc, 0, v19, vcc
	global_load_dwordx4 v[2:5], v34, s[70:71] offset:16
	global_load_dwordx4 v[6:9], v34, s[70:71]
	global_load_dwordx4 v[10:13], v34, s[70:71] offset:2064
	global_load_dwordx4 v[14:17], v34, s[70:71] offset:2048
	global_load_dwordx4 v[18:21], v[22:23], off
	s_nop 0
	global_load_dwordx4 v[22:25], v[22:23], off offset:2048
	s_nop 0
	global_load_dwordx4 v[26:29], v[26:27], off offset:16
	s_nop 0
	global_load_dwordx4 v[30:33], v[30:31], off offset:16
	v_mbcnt_lo_u32_b32 v1, -1, 0
	v_mbcnt_hi_u32_b32 v1, -1, v1
	v_and_b32_e32 v36, 64, v1
	v_add_u32_e32 v36, 64, v36
	v_xor_b32_e32 v37, 1, v1
	v_cmp_lt_i32_e32 vcc, v37, v36
	s_ashr_i32 s11, s10, 31
	s_lshl_b64 s[4:5], s[10:11], 13
	v_cndmask_b32_e32 v37, v1, v37, vcc
	v_lshlrev_b32_e32 v70, 2, v37
	v_xor_b32_e32 v37, 2, v1
	v_cmp_lt_i32_e32 vcc, v37, v36
	s_add_u32 s4, s68, s4
	s_addc_u32 s5, s69, s5
	v_cndmask_b32_e32 v37, v1, v37, vcc
	v_lshlrev_b32_e32 v71, 2, v37
	v_xor_b32_e32 v37, 4, v1
	v_cmp_lt_i32_e32 vcc, v37, v36
	s_ashr_i32 s13, s12, 31
	s_lshl_b64 s[14:15], s[12:13], 13
	v_cndmask_b32_e32 v37, v1, v37, vcc
	v_lshlrev_b32_e32 v72, 2, v37
	v_xor_b32_e32 v37, 8, v1
	v_cmp_lt_i32_e32 vcc, v37, v36
	v_mov_b32_e32 v76, 0x358637bd
	v_mov_b32_e32 v77, 0x260
	v_cndmask_b32_e32 v37, v1, v37, vcc
	v_lshlrev_b32_e32 v73, 2, v37
	v_xor_b32_e32 v37, 16, v1
	v_cmp_lt_i32_e32 vcc, v37, v36
	s_nop 1
	v_cndmask_b32_e32 v37, v1, v37, vcc
	v_lshlrev_b32_e32 v74, 2, v37
	v_xor_b32_e32 v37, 32, v1
	v_cmp_lt_i32_e32 vcc, v37, v36
	s_nop 1
	v_cndmask_b32_e32 v1, v1, v37, vcc
	v_lshl_add_u64 v[36:37], s[4:5], 0, v[34:35]
	v_lshl_add_u64 v[66:67], v[36:37], 0, s[2:3]
	s_lshl_b64 s[2:3], s[10:11], 12
	s_add_u32 s2, s28, s2
	v_lshlrev_b32_e32 v34, 4, v38
	s_addc_u32 s3, s29, s3
	v_lshl_add_u64 v[34:35], s[2:3], 0, v[34:35]
	s_mov_b64 s[2:3], 0x2a300000
	v_lshlrev_b32_e32 v75, 2, v1
	v_lshl_add_u64 v[68:69], v[34:35], 0, s[2:3]
	s_lshl_b64 s[16:17], s[12:13], 12
	s_mov_b32 s2, 0xf800000
	global_load_dwordx4 v[110:113], v[66:67], off offset:-2048
	global_load_dwordx4 v[114:117], v[66:67], off offset:16
	global_load_dwordx4 v[122:125], v[66:67], off offset:-4096
	global_load_dwordx4 v[118:121], v[66:67], off offset:-4080
	global_load_dwordx4 v[130:133], v[66:67], off offset:-2032
	global_load_dwordx4 v[126:129], v[66:67], off
	global_load_dwordx4 v[138:141], v[66:67], off offset:2048
	global_load_dwordx4 v[134:137], v[66:67], off offset:2064
	v_lshl_add_u64 v[66:67], v[66:67], 0, s[14:15]
	s_waitcnt vmcnt(0)
.LBB0_13:
	s_waitcnt vmcnt(4)
	v_mov_b32_e32 v34, v110
	v_mov_b32_e32 v35, v111
	v_mov_b32_e32 v36, v112
	v_mov_b32_e32 v37, v113
	v_mov_b32_e32 v38, v114
	v_mov_b32_e32 v39, v115
	v_mov_b32_e32 v40, v116
	v_mov_b32_e32 v41, v117
	v_mov_b32_e32 v42, v118
	v_mov_b32_e32 v43, v119
	v_mov_b32_e32 v44, v120
	v_mov_b32_e32 v45, v121
	v_mov_b32_e32 v46, v122
	v_mov_b32_e32 v47, v123
	v_mov_b32_e32 v48, v124
	v_mov_b32_e32 v49, v125
	v_mov_b32_e32 v50, v126
	v_mov_b32_e32 v51, v127
	v_mov_b32_e32 v52, v128
	v_mov_b32_e32 v53, v129
	v_mov_b32_e32 v54, v130
	v_mov_b32_e32 v55, v131
	v_mov_b32_e32 v56, v132
	v_mov_b32_e32 v57, v133
	v_mov_b32_e32 v58, v134
	v_mov_b32_e32 v59, v135
	v_mov_b32_e32 v60, v136
	v_mov_b32_e32 v61, v137
	v_mov_b32_e32 v62, v138
	v_mov_b32_e32 v63, v139
	v_mov_b32_e32 v64, v140
	v_mov_b32_e32 v65, v141
	s_add_i32 s10, s10, s12
	s_cmpk_gt_i32 s10, 0x3fff
	s_cbranch_scc1 .Lp0_nopf
	global_load_dwordx4 v[110:113], v[66:67], off offset:-2048
	global_load_dwordx4 v[114:117], v[66:67], off offset:16
	global_load_dwordx4 v[122:125], v[66:67], off offset:-4096
	global_load_dwordx4 v[118:121], v[66:67], off offset:-4080
	global_load_dwordx4 v[130:133], v[66:67], off offset:-2032
	global_load_dwordx4 v[126:129], v[66:67], off
	global_load_dwordx4 v[138:141], v[66:67], off offset:2048
	global_load_dwordx4 v[134:137], v[66:67], off offset:2064
	v_lshl_add_u64 v[66:67], v[66:67], 0, s[14:15]
.Lp0_nopf:
	v_pk_mul_f32 v[78:79], v[36:37], v[36:37]
	v_pk_mul_f32 v[80:81], v[34:35], v[34:35]
	v_pk_mul_f32 v[82:83], v[40:41], v[40:41]
	v_pk_mul_f32 v[84:85], v[38:39], v[38:39]
	v_mov_b32_e32 v88, v47
	v_mov_b32_e32 v89, v43
	v_mov_b32_e32 v92, v49
	v_mov_b32_e32 v93, v45
	v_mov_b32_e32 v86, v46
	v_mov_b32_e32 v87, v42
	v_mov_b32_e32 v90, v48
	v_mov_b32_e32 v91, v44
	v_pk_mov_b32 v[102:103], v[80:81], v[78:79] op_sel:[1,0]
	v_mov_b32_e32 v81, v79
	v_pk_mov_b32 v[78:79], v[84:85], v[82:83] op_sel:[1,0]
	v_mov_b32_e32 v85, v83
	v_pk_mul_f32 v[82:83], v[88:89], v[88:89]
	v_pk_mul_f32 v[88:89], v[92:93], v[92:93]
	v_pk_fma_f32 v[82:83], v[86:87], v[86:87], v[82:83]
	v_pk_fma_f32 v[86:87], v[90:91], v[90:91], v[88:89]
	v_mul_f32_e32 v94, v55, v55
	v_mul_f32_e32 v96, v57, v57
	v_pk_add_f32 v[80:81], v[102:103], v[80:81]
	v_pk_add_f32 v[82:83], v[82:83], v[86:87]
	v_mul_f32_e32 v1, v52, v52
	v_mul_f32_e32 v101, v53, v53
	v_mul_f32_e32 v106, v51, v51
	v_mul_f32_e32 v107, v50, v50
	v_pk_fma_f32 v[92:93], v[54:55], v[54:55], v[94:95] op_sel_hi:[1,1,0]
	v_pk_fma_f32 v[94:95], v[56:57], v[56:57], v[96:97] op_sel_hi:[1,1,0]
	v_pk_add_f32 v[80:81], v[80:81], v[80:81] op_sel:[0,1] op_sel_hi:[1,0]
	v_pk_add_f32 v[82:83], v[82:83], v[82:83] op_sel:[0,1] op_sel_hi:[1,0]
	v_mov_b32_e32 v93, v1
	v_mov_b32_e32 v95, v101
	v_mov_b32_e32 v81, v106
	v_mov_b32_e32 v83, v107
	v_pk_add_f32 v[78:79], v[78:79], v[84:85]
	v_pk_add_f32 v[84:85], v[92:93], v[94:95]
	v_pk_add_f32 v[80:81], v[82:83], v[80:81]
	v_mul_f32_e32 v98, v63, v63
	v_mul_f32_e32 v100, v65, v65
	v_pk_add_f32 v[80:81], v[80:81], v[84:85]
	v_mul_f32_e32 v104, v60, v60
	v_mul_f32_e32 v105, v61, v61
	v_mul_f32_e32 v108, v59, v59
	v_mul_f32_e32 v109, v58, v58
	v_pk_fma_f32 v[96:97], v[62:63], v[62:63], v[98:99] op_sel_hi:[1,1,0]
	v_pk_fma_f32 v[98:99], v[64:65], v[64:65], v[100:101] op_sel_hi:[1,1,0]
	v_pk_add_f32 v[78:79], v[78:79], v[78:79] op_sel:[0,1] op_sel_hi:[1,0]
	v_pk_add_f32 v[80:81], v[80:81], v[80:81] op_sel:[0,1] op_sel_hi:[1,0]
	v_mov_b32_e32 v97, v104
	v_mov_b32_e32 v99, v105
	v_mov_b32_e32 v79, v108
	v_mov_b32_e32 v81, v109
	v_pk_add_f32 v[86:87], v[96:97], v[98:99]
	v_pk_add_f32 v[78:79], v[80:81], v[78:79]
	s_nop 0
	v_pk_add_f32 v[78:79], v[78:79], v[86:87]
	s_nop 0
	v_add_f32_e32 v1, v78, v79
	ds_bpermute_b32 v78, v70, v1
	s_waitcnt lgkmcnt(0)
	v_add_f32_e32 v1, v1, v78
	ds_bpermute_b32 v78, v71, v1
	s_waitcnt lgkmcnt(0)
	v_add_f32_e32 v1, v1, v78
	ds_bpermute_b32 v78, v72, v1
	s_waitcnt lgkmcnt(0)
	v_add_f32_e32 v1, v1, v78
	ds_bpermute_b32 v78, v73, v1
	s_waitcnt lgkmcnt(0)
	v_add_f32_e32 v1, v1, v78
	ds_bpermute_b32 v78, v74, v1
	s_waitcnt lgkmcnt(0)
	v_add_f32_e32 v1, v1, v78
	ds_bpermute_b32 v78, v75, v1
	s_waitcnt lgkmcnt(0)
	v_add_f32_e32 v1, v1, v78
	v_fmamk_f32 v1, v1, 0x3a000000, v76
	v_mul_f32_e32 v78, 0x4f800000, v1
	v_cmp_gt_f32_e32 vcc, s2, v1
	s_nop 1
	v_cndmask_b32_e32 v1, v1, v78, vcc
	v_sqrt_f32_e32 v78, v1
	s_nop 0
	v_add_u32_e32 v79, -1, v78
	v_add_u32_e32 v80, 1, v78
	v_fma_f32 v81, -v79, v78, v1
	v_fma_f32 v82, -v80, v78, v1
	v_cmp_ge_f32_e64 s[4:5], 0, v81
	s_nop 1
	v_cndmask_b32_e64 v78, v78, v79, s[4:5]
	v_cmp_lt_f32_e64 s[4:5], 0, v82
	s_nop 1
	v_cndmask_b32_e64 v78, v78, v80, s[4:5]
	v_mul_f32_e32 v79, 0x37800000, v78
	v_cndmask_b32_e32 v78, v78, v79, vcc
	v_cmp_class_f32_e32 vcc, v1, v77
	s_nop 1
	v_cndmask_b32_e32 v1, v78, v1, vcc
	v_div_scale_f32 v78, s[4:5], v1, v1, 1.0
	v_rcp_f32_e32 v80, v78
	v_div_scale_f32 v79, vcc, 1.0, v1, 1.0
	v_fma_f32 v81, -v78, v80, 1.0
	v_fmac_f32_e32 v80, v81, v80
	v_mul_f32_e32 v81, v79, v80
	v_fma_f32 v82, -v78, v81, v79
	v_fmac_f32_e32 v81, v82, v80
	v_fma_f32 v78, -v78, v81, v79
	v_div_fmas_f32 v78, v78, v80, v81
	v_div_fixup_f32 v78, v78, v1, 1.0
	v_pk_mul_f32 v[46:47], v[46:47], v[78:79] op_sel_hi:[1,0]
	v_pk_mul_f32 v[48:49], v[48:49], v[78:79] op_sel_hi:[1,0]
	v_pk_mul_f32 v[42:43], v[42:43], v[78:79] op_sel_hi:[1,0]
	v_pk_mul_f32 v[44:45], v[44:45], v[78:79] op_sel_hi:[1,0]
	v_pk_mul_f32 v[34:35], v[34:35], v[78:79] op_sel_hi:[1,0]
	v_pk_mul_f32 v[36:37], v[36:37], v[78:79] op_sel_hi:[1,0]
	v_pk_mul_f32 v[54:55], v[54:55], v[78:79] op_sel_hi:[1,0]
	v_pk_mul_f32 v[56:57], v[56:57], v[78:79] op_sel_hi:[1,0]
	v_pk_mul_f32 v[50:51], v[50:51], v[78:79] op_sel_hi:[1,0]
	v_pk_mul_f32 v[52:53], v[52:53], v[78:79] op_sel_hi:[1,0]
	v_pk_mul_f32 v[38:39], v[38:39], v[78:79] op_sel_hi:[1,0]
	v_pk_mul_f32 v[40:41], v[40:41], v[78:79] op_sel_hi:[1,0]
	v_pk_mul_f32 v[62:63], v[62:63], v[78:79] op_sel_hi:[1,0]
	v_pk_mul_f32 v[64:65], v[64:65], v[78:79] op_sel_hi:[1,0]
	v_pk_mul_f32 v[58:59], v[58:59], v[78:79] op_sel_hi:[1,0]
	v_pk_mul_f32 v[60:61], v[60:61], v[78:79] op_sel_hi:[1,0]
	v_pk_mul_f32 v[48:49], v[8:9], v[48:49]
	v_pk_mul_f32 v[46:47], v[6:7], v[46:47]
	v_pk_mul_f32 v[42:43], v[2:3], v[42:43]
	v_pk_mul_f32 v[44:45], v[4:5], v[44:45]
	v_pk_mul_f32 v[78:79], v[16:17], v[36:37]
	v_pk_mul_f32 v[80:81], v[14:15], v[34:35]
	v_pk_mul_f32 v[54:55], v[10:11], v[54:55]
	v_pk_mul_f32 v[56:57], v[12:13], v[56:57]
	v_pk_mul_f32 v[52:53], v[20:21], v[52:53]
	v_pk_mul_f32 v[50:51], v[18:19], v[50:51]
	v_pk_mul_f32 v[82:83], v[28:29], v[40:41]
	v_pk_mul_f32 v[84:85], v[26:27], v[38:39]
	v_pk_mul_f32 v[64:65], v[24:25], v[64:65]
	v_pk_mul_f32 v[62:63], v[22:23], v[62:63]
	v_pk_mul_f32 v[60:61], v[32:33], v[60:61]
	v_pk_mul_f32 v[58:59], v[30:31], v[58:59]
	v_cvt_pk_bf16_f32 v34, v46, v47
	v_cvt_pk_bf16_f32 v35, v48, v49
	v_cvt_pk_bf16_f32 v36, v42, v43
	v_cvt_pk_bf16_f32 v37, v44, v45
	v_cvt_pk_bf16_f32 v38, v80, v81
	v_cvt_pk_bf16_f32 v39, v78, v79
	v_cvt_pk_bf16_f32 v40, v54, v55
	v_cvt_pk_bf16_f32 v41, v56, v57
	v_cvt_pk_bf16_f32 v42, v50, v51
	v_cvt_pk_bf16_f32 v43, v52, v53
	v_cvt_pk_bf16_f32 v44, v84, v85
	v_cvt_pk_bf16_f32 v45, v82, v83
	v_cvt_pk_bf16_f32 v46, v62, v63
	v_cvt_pk_bf16_f32 v47, v64, v65
	v_cvt_pk_bf16_f32 v48, v58, v59
	v_cvt_pk_bf16_f32 v49, v60, v61
	global_store_dwordx4 v[68:69], v[34:37], off
	global_store_dwordx4 v[68:69], v[38:41], off offset:1024
	global_store_dwordx4 v[68:69], v[42:45], off offset:2048
	global_store_dwordx4 v[68:69], v[46:49], off offset:3072
	v_lshl_add_u64 v[68:69], v[68:69], 0, s[16:17]
	s_cbranch_scc0 .LBB0_13
